# mixer: output addresses advanced before the stores (no register write right behind a store)
# baseline (speedup 1.0000x reference)
.LBB0_464:
	s_ashr_i32 s8, s24, 2
	s_add_i32 s24, s8, s78
	s_lshl_b32 s8, s79, 7
	s_and_b64 s[78:79], s[76:77], exec
	s_movk_i32 s9, 0x1500
	s_cselect_b32 s9, s9, 0x1800
	s_and_b64 s[6:7], exec, s[6:7]
	s_cselect_b32 s6, 0x900, s9
	s_lshl_b32 s2, s2, 6
	s_and_b32 s40, s2, 64
	s_add_i32 s7, s81, s8
	s_or_b32 s78, s7, s40
	s_ashr_i32 s7, s5, 31
	s_lshr_b32 s7, s7, 30
	s_add_i32 s7, s5, s7
	s_and_b32 s7, s7, 0x1ffffc
	s_sub_i32 s5, s5, s7
	s_lshl_b32 s84, s5, 11
	v_cndmask_b32_e64 v3, v111, v110, s[76:77]
	v_add_u32_e32 v3, s84, v3
	s_add_i32 s2, s80, s8
	v_mad_i64_i32 v[4:5], s[80:81], v3, s20, v[38:39]
	s_add_i32 s6, s6, s8
	s_mov_b32 s7, s3
	s_lshl_b64 s[80:81], s[2:3], 1
	s_mov_b32 m0, s19
	v_lshl_add_u64 v[6:7], v[4:5], 0, s[80:81]
	s_lshl_b64 s[6:7], s[6:7], 1
	v_cndmask_b32_e64 v3, v113, v112, s[76:77]
	s_waitcnt vmcnt(0) lgkmcnt(0)
	s_barrier
	global_load_lds_dwordx4 v[6:7], off
	v_lshl_add_u64 v[4:5], v[4:5], 0, s[6:7]
	s_mov_b32 m0, s82
	v_add_u32_e32 v3, s84, v3
	global_load_lds_dwordx4 v[4:5], off
	v_mad_i64_i32 v[4:5], s[86:87], v3, s20, v[38:39]
	s_add_i32 s85, s92, 0x1b600
	v_lshl_add_u64 v[6:7], v[4:5], 0, s[80:81]
	s_mov_b32 m0, s85
	s_add_i32 s86, s92, 0x1f600
	global_load_lds_dwordx4 v[6:7], off
	v_lshl_add_u64 v[4:5], v[4:5], 0, s[6:7]
	s_mov_b32 m0, s86
	v_cndmask_b32_e64 v3, v101, v100, s[76:77]
	global_load_lds_dwordx4 v[4:5], off
	v_add_u32_e32 v3, s84, v3
	v_mov_b64_e32 v[4:5], s[26:27]
	s_mov_b32 s79, s3
	v_mad_i64_i32 v[4:5], vcc, v3, s20, v[4:5]
	s_lshl_b64 s[78:79], s[78:79], 1
	s_add_i32 s87, s16, 0
	v_lshl_add_u64 v[4:5], v[4:5], 0, s[78:79]
	v_mov_b32_e32 v45, v195
	s_add_i32 s87, s87, 0x23600
	v_lshl_add_u64 v[4:5], v[4:5], 0, v[44:45]
	s_mov_b32 m0, s87
	v_mul_f32_e32 v144, 0x42800000, v2
	global_load_lds_dwordx4 v[4:5], off
	v_mul_f32_e32 v2, 0x42000000, v2
	v_exp_f32_e32 v18, v2
	s_ashr_i32 s9, s8, 31
	s_waitcnt vmcnt(0)
	s_lshl_b32 s2, s4, 13
	v_mad_i64_i32 v[2:3], s[4:5], s24, v242, v[42:43]
	v_lshl_add_u64 v[2:3], s[8:9], 1, v[2:3]
	s_lshl_b32 s4, s40, 1
	s_mov_b32 s5, s3
	v_mov_b32_e32 v22, 0
	v_lshl_add_u64 v[52:53], v[40:41], 0, s[78:79]
	v_sub_f32_e32 v45, 1.0, v140
	v_sub_f32_e32 v143, 1.0, v139
	v_lshl_add_u64 v[54:55], v[2:3], 0, s[4:5]
	v_mov_b32_e32 v47, v46
	s_mov_b32 s24, 0
	v_mov_b32_e32 v19, v18
	v_mov_b32_e32 v20, v18
	v_mov_b32_e32 v21, v18
	s_mov_b32 s4, 0
	v_mov_b32_e32 v23, v22
	v_mov_b32_e32 v24, v22
	v_mov_b32_e32 v25, v22
	v_mov_b32_e32 v26, v22
	v_mov_b32_e32 v27, v22
	v_mov_b32_e32 v28, v22
	v_mov_b32_e32 v29, v22
	v_mov_b32_e32 v30, v22
	v_mov_b32_e32 v31, v22
	v_mov_b32_e32 v32, v22
	v_mov_b32_e32 v33, v22
	v_mov_b32_e32 v34, v22
	v_mov_b32_e32 v35, v22
	v_mov_b32_e32 v36, v22
	v_mov_b32_e32 v37, v22
	v_add_u32_e32 v177, s24, v118
	v_add_u32_e32 v176, s4, v109
	v_add_u32_e32 v178, 0x7ff, v177
	v_cndmask_b32_e64 v178, v178, v176, s[76:77]
	v_or_b32_e32 v180, s84, v178
	v_ashrrev_i32_e32 v181, 31, v180
	v_lshl_add_u64 v[180:181], v[180:181], 0, s[2:3]
	v_mad_u64_u32 v[192:193], s[8:9], v180, s11, v[54:55]
	v_mad_i32_i24 v193, v181, s11, v193
	v_add_u32_e32 v182, 16, v176
	v_add_u32_e32 v183, 0x7ef, v177
	v_cndmask_b32_e64 v182, v183, v182, s[76:77]
	v_or_b32_e32 v184, s84, v182
	v_ashrrev_i32_e32 v185, 31, v184
	v_lshl_add_u64 v[184:185], v[184:185], 0, s[2:3]
	v_mad_u64_u32 v[216:217], s[8:9], v184, s11, v[54:55]
	v_mad_i32_i24 v217, v185, s11, v217
	v_mov_b32_e32 v186, s11
	v_lshlrev_b32_e32 v186, 6, v186
	v_sub_u32_e32 v187, 0, v186
	v_cndmask_b32_e64 v244, v187, v186, s[76:77]
	v_cndmask_b32_e64 v245, -1, 0, s[76:77]
	v_cndmask_b32_e64 v188, v186, v187, s[76:77]
	v_cndmask_b32_e64 v189, 0, -1, s[76:77]
	v_lshl_add_u64 v[192:193], v[192:193], 0, v[188:189]
	v_lshl_add_u64 v[216:217], v[216:217], 0, v[188:189]
	s_waitcnt vmcnt(0) lgkmcnt(0)
	s_barrier
	s_branch .LBB0_466
.LBB0_465:
	s_waitcnt lgkmcnt(0)
	s_barrier
	ds_read_b128 v[10:13], v127
	ds_read_b128 v[14:17], v127 offset:64
	ds_read_b128 v[56:59], v127 offset:128
	ds_read_b128 v[60:63], v127 offset:192
	ds_read_b128 v[64:67], v128 offset:17408
	ds_read_b128 v[68:71], v128 offset:17472
	ds_read_b128 v[72:75], v128 offset:17536
	ds_read_b128 v[76:79], v128 offset:17600
	ds_read_b128 v[176:179], v128 offset:21760
	ds_read_b128 v[180:183], v128 offset:21824
	ds_read_b128 v[184:187], v128 offset:21888
	ds_read_b128 v[188:191], v128 offset:21952
	s_waitcnt lgkmcnt(7)
	v_mfma_f32_16x16x32_bf16 v[2:5], v[64:67], v[10:13], 0
	s_waitcnt lgkmcnt(6)
	v_mfma_f32_16x16x32_bf16 v[2:5], v[68:71], v[14:17], v[2:5]
	s_waitcnt lgkmcnt(3)
	v_mfma_f32_16x16x32_bf16 v[6:9], v[176:179], v[10:13], 0
	v_mfma_f32_16x16x32_bf16 v[2:5], v[72:75], v[56:59], v[2:5]
	s_waitcnt lgkmcnt(2)
	v_mfma_f32_16x16x32_bf16 v[6:9], v[180:183], v[14:17], v[6:9]
	v_mfma_f32_16x16x32_bf16 v[2:5], v[76:79], v[60:63], v[2:5]
	s_waitcnt lgkmcnt(1)
	v_mfma_f32_16x16x32_bf16 v[6:9], v[184:187], v[56:59], v[6:9]
	s_waitcnt lgkmcnt(0)
	v_mfma_f32_16x16x32_bf16 v[6:9], v[188:191], v[60:63], v[6:9]
	s_nop 6
	v_cndmask_b32_e64 v56, v2, 0, s[44:45]
	v_cndmask_b32_e64 v57, 0, v3, s[46:47]
	v_cndmask_b32_e64 v58, v4, 0, s[48:49]
	v_cndmask_b32_e64 v59, v5, 0, s[50:51]
	v_cvt_pk_bf16_f32 v56, v56, v57
	v_cvt_pk_bf16_f32 v57, v58, v59
	ds_write_b64 v129, v[56:57]
	v_cndmask_b32_e64 v6, v6, 0, s[52:53]
	v_cndmask_b32_e64 v7, 0, v7, s[54:55]
	v_cndmask_b32_e64 v8, v8, 0, s[56:57]
	v_cndmask_b32_e64 v9, v9, 0, s[58:59]
	v_cvt_pk_bf16_f32 v6, v6, v7
	v_cvt_pk_bf16_f32 v7, v8, v9
	ds_write_b64 v130, v[6:7]
	s_waitcnt lgkmcnt(0)
	s_barrier
	ds_read_b128 v[10:13], v131
	ds_read_b128 v[14:17], v132
	ds_read_b128 v[56:59], v133
	ds_read_b128 v[60:63], v131 offset:64
	ds_read_b128 v[64:67], v132 offset:64
	ds_read_b128 v[68:71], v133 offset:64
	ds_read_b128 v[72:75], v138
	ds_read_b128 v[76:79], v134 offset:52224
	ds_read_b128 v[176:179], v137
	ds_read_b128 v[180:183], v137 offset:2304
	ds_read_b128 v[184:187], v137 offset:4608
	ds_read_b128 v[188:191], v137 offset:6912
	ds_read_b128 v[200:203], v134 offset:52288
	ds_read_b128 v[204:207], v137 offset:64
	ds_read_b128 v[208:211], v137 offset:2368
	s_waitcnt lgkmcnt(13)
	v_mfma_f32_16x16x32_bf16 v[6:9], v[10:13], v[14:17], 0
	s_waitcnt lgkmcnt(12)
	v_mfma_f32_16x16x32_bf16 v[2:5], v[10:13], v[56:59], 0
	ds_read_b128 v[212:215], v137 offset:4672
	ds_read_b128 v[220:223], v137 offset:6976
	ds_read_b128 v[224:227], v135
	s_waitcnt lgkmcnt(13)
	v_mfma_f32_16x16x32_bf16 v[6:9], v[60:63], v[64:67], v[6:9]
	s_waitcnt lgkmcnt(12)
	v_mfma_f32_16x16x32_bf16 v[2:5], v[60:63], v[68:71], v[2:5]
	ds_read_b128 v[232:235], v128
	ds_read_b128 v[236:239], v136
	ds_read_b128 v[14:17], v135 offset:64
	s_waitcnt lgkmcnt(14)
	v_pk_mul_f32 v[22:23], v[22:23], v[72:73]
	v_pk_mul_f32 v[24:25], v[24:25], v[74:75]
	v_pk_mul_f32 v[26:27], v[26:27], v[72:73]
	v_pk_mul_f32 v[28:29], v[28:29], v[74:75]
	v_pk_mul_f32 v[30:31], v[30:31], v[72:73]
	v_pk_mul_f32 v[32:33], v[32:33], v[74:75]
	v_pk_mul_f32 v[34:35], v[34:35], v[72:73]
	v_pk_mul_f32 v[36:37], v[36:37], v[74:75]
	s_waitcnt lgkmcnt(12)
	v_mfma_f32_16x16x32_bf16 v[22:25], v[76:79], v[176:179], v[22:25]
	s_waitcnt lgkmcnt(11)
	v_mfma_f32_16x16x32_bf16 v[26:29], v[76:79], v[180:183], v[26:29]
	s_waitcnt lgkmcnt(10)
	v_mfma_f32_16x16x32_bf16 v[30:33], v[76:79], v[184:187], v[30:33]
	s_waitcnt lgkmcnt(9)
	v_mfma_f32_16x16x32_bf16 v[34:37], v[76:79], v[188:191], v[34:37]
	ds_read_b128 v[10:13], v128 offset:64
	ds_read_b128 v[56:59], v136 offset:64
	ds_read_b128 v[64:67], v135 offset:128
	ds_read_b128 v[60:63], v128 offset:128
	s_waitcnt lgkmcnt(11)
	v_mfma_f32_16x16x32_bf16 v[22:25], v[200:203], v[204:207], v[22:25]
	s_waitcnt lgkmcnt(10)
	v_mfma_f32_16x16x32_bf16 v[26:29], v[200:203], v[208:211], v[26:29]
	ds_read_b128 v[68:71], v136 offset:128
	ds_read_b128 v[72:75], v135 offset:192
	s_waitcnt lgkmcnt(11)
	v_mfma_f32_16x16x32_bf16 v[30:33], v[200:203], v[212:215], v[30:33]
	s_waitcnt lgkmcnt(10)
	v_mfma_f32_16x16x32_bf16 v[34:37], v[200:203], v[220:223], v[34:37]
	ds_read_b128 v[176:179], v128 offset:192
	ds_read_b128 v[180:183], v136 offset:192
	s_waitcnt lgkmcnt(10)
	v_mfma_f32_16x16x32_bf16 v[6:9], v[224:227], v[232:235], v[6:9]
	s_waitcnt lgkmcnt(9)
	v_mfma_f32_16x16x32_bf16 v[2:5], v[224:227], v[236:239], v[2:5]
	s_waitcnt lgkmcnt(7)
	v_mfma_f32_16x16x32_bf16 v[6:9], v[14:17], v[10:13], v[6:9]
	s_waitcnt lgkmcnt(6)
	v_mfma_f32_16x16x32_bf16 v[2:5], v[14:17], v[56:59], v[2:5]
	s_waitcnt lgkmcnt(4)
	v_mfma_f32_16x16x32_bf16 v[6:9], v[64:67], v[60:63], v[6:9]
	s_waitcnt lgkmcnt(3)
	v_mfma_f32_16x16x32_bf16 v[2:5], v[64:67], v[68:71], v[2:5]
	s_waitcnt lgkmcnt(1)
	v_mfma_f32_16x16x32_bf16 v[6:9], v[72:75], v[176:179], v[6:9]
	s_waitcnt lgkmcnt(0)
	v_mfma_f32_16x16x32_bf16 v[2:5], v[72:75], v[180:183], v[2:5]
	s_add_i32 s4, s4, 64
	s_sub_i32 s24, s24, 64
	s_cmpk_eq_i32 s4, 0x800
	s_waitcnt vmcnt(1)
	v_lshl_add_u64 v[192:193], v[192:193], 0, v[244:245]
	v_lshl_add_u64 v[216:217], v[216:217], 0, v[244:245]
	s_nop 5
	v_cvt_pk_bf16_f32 v6, v6, v7
	v_cvt_pk_bf16_f32 v7, v8, v9
	global_store_dwordx2 v[192:193], v[6:7], off
	v_cvt_pk_bf16_f32 v2, v2, v3
	v_cvt_pk_bf16_f32 v3, v4, v5
	global_store_dwordx2 v[216:217], v[2:3], off
	s_cbranch_scc1 .LBB0_448
